# t24
# speedup vs baseline: 1.0031x; 1.0031x over previous
.Ljoin:
	s_barrier
	v_mov_b32_e32 v6, 0x6000
	ds_read_b96 v[32:34], v6
	ds_read_b96 v[36:38], v6 offset:16
	ds_read_b96 v[40:42], v6 offset:32
	ds_read_b96 v[44:46], v6 offset:48
	v_add_u32_e32 v56, 0xc00, v3
	v_add_u32_e32 v57, 0x1200, v3
	ds_read2_b32 v[8:9], v3 offset0:0 offset1:1
	ds_read_b32 v24, v3 offset:8
	ds_read2_b32 v[10:11], v3 offset0:192 offset1:193
	ds_read_b32 v25, v3 offset:776
	ds_read2_b32 v[12:13], v4 offset0:0 offset1:1
	ds_read_b32 v26, v4 offset:8
	s_waitcnt lgkmcnt(4)
	v_fma_f32 v60, v8, v32, v44
	v_fma_f32 v61, v8, v33, v45
	v_fma_f32 v62, v8, v34, v46
	v_fmac_f32_e32 v60, v9, v36
	v_fmac_f32_e32 v61, v9, v37
	v_fmac_f32_e32 v62, v9, v38
	v_fmac_f32_e32 v60, v24, v40
	v_fmac_f32_e32 v61, v24, v41
	v_fmac_f32_e32 v62, v24, v42
	ds_write2_b32 v3, v60, v61 offset0:0 offset1:1
	ds_write_b32 v3, v62 offset:8
	ds_read2_b32 v[14:15], v4 offset0:192 offset1:193
	ds_read_b32 v27, v4 offset:776
	s_waitcnt lgkmcnt(6)
	v_fma_f32 v35, v10, v32, v44
	v_fma_f32 v39, v10, v33, v45
	v_fma_f32 v43, v10, v34, v46
	v_fmac_f32_e32 v35, v11, v36
	v_fmac_f32_e32 v39, v11, v37
	v_fmac_f32_e32 v43, v11, v38
	v_fmac_f32_e32 v35, v25, v40
	v_fmac_f32_e32 v39, v25, v41
	v_fmac_f32_e32 v43, v25, v42
	ds_write2_b32 v3, v35, v39 offset0:192 offset1:193
	ds_write_b32 v3, v43 offset:776
	ds_read2_b32 v[16:17], v56 offset0:0 offset1:1
	ds_read_b32 v28, v56 offset:8
	s_waitcnt lgkmcnt(8)
	v_fma_f32 v60, v12, v32, v44
	v_fma_f32 v61, v12, v33, v45
	v_fma_f32 v62, v12, v34, v46
	v_fmac_f32_e32 v60, v13, v36
	v_fmac_f32_e32 v61, v13, v37
	v_fmac_f32_e32 v62, v13, v38
	v_fmac_f32_e32 v60, v26, v40
	v_fmac_f32_e32 v61, v26, v41
	v_fmac_f32_e32 v62, v26, v42
	ds_write2_b32 v4, v60, v61 offset0:0 offset1:1
	ds_write_b32 v4, v62 offset:8
	ds_read2_b32 v[18:19], v56 offset0:192 offset1:193
	ds_read_b32 v29, v56 offset:776
	s_waitcnt lgkmcnt(8)
	v_fma_f32 v35, v14, v32, v44
	v_fma_f32 v39, v14, v33, v45
	v_fma_f32 v43, v14, v34, v46
	v_fmac_f32_e32 v35, v15, v36
	v_fmac_f32_e32 v39, v15, v37
	v_fmac_f32_e32 v43, v15, v38
	v_fmac_f32_e32 v35, v27, v40
	v_fmac_f32_e32 v39, v27, v41
	v_fmac_f32_e32 v43, v27, v42
	ds_write2_b32 v4, v35, v39 offset0:192 offset1:193
	ds_write_b32 v4, v43 offset:776
	ds_read2_b32 v[20:21], v57 offset0:0 offset1:1
	ds_read_b32 v30, v57 offset:8
	s_waitcnt lgkmcnt(8)
	v_fma_f32 v60, v16, v32, v44
	v_fma_f32 v61, v16, v33, v45
	v_fma_f32 v62, v16, v34, v46
	v_fmac_f32_e32 v60, v17, v36
	v_fmac_f32_e32 v61, v17, v37
	v_fmac_f32_e32 v62, v17, v38
	v_fmac_f32_e32 v60, v28, v40
	v_fmac_f32_e32 v61, v28, v41
	v_fmac_f32_e32 v62, v28, v42
	ds_write2_b32 v56, v60, v61 offset0:0 offset1:1
	ds_write_b32 v56, v62 offset:8
	ds_read2_b32 v[22:23], v57 offset0:192 offset1:193
	ds_read_b32 v31, v57 offset:776
	s_waitcnt lgkmcnt(8)
	v_fma_f32 v35, v18, v32, v44
	v_fma_f32 v39, v18, v33, v45
	v_fma_f32 v43, v18, v34, v46
	v_fmac_f32_e32 v35, v19, v36
	v_fmac_f32_e32 v39, v19, v37
	v_fmac_f32_e32 v43, v19, v38
	v_fmac_f32_e32 v35, v29, v40
	v_fmac_f32_e32 v39, v29, v41
	v_fmac_f32_e32 v43, v29, v42
	ds_write2_b32 v56, v35, v39 offset0:192 offset1:193
	ds_write_b32 v56, v43 offset:776
	s_waitcnt lgkmcnt(6)
	v_fma_f32 v60, v20, v32, v44
	v_fma_f32 v61, v20, v33, v45
	v_fma_f32 v62, v20, v34, v46
	v_fmac_f32_e32 v60, v21, v36
	v_fmac_f32_e32 v61, v21, v37
	v_fmac_f32_e32 v62, v21, v38
	v_fmac_f32_e32 v60, v30, v40
	v_fmac_f32_e32 v61, v30, v41
	v_fmac_f32_e32 v62, v30, v42
	ds_write2_b32 v57, v60, v61 offset0:0 offset1:1
	ds_write_b32 v57, v62 offset:8
	s_waitcnt lgkmcnt(4)
	v_fma_f32 v35, v22, v32, v44
	v_fma_f32 v39, v22, v33, v45
	v_fma_f32 v43, v22, v34, v46
	v_fmac_f32_e32 v35, v23, v36
	v_fmac_f32_e32 v39, v23, v37
	v_fmac_f32_e32 v43, v23, v38
	v_fmac_f32_e32 v35, v31, v40
	v_fmac_f32_e32 v39, v31, v41
	v_fmac_f32_e32 v43, v31, v42
	ds_write2_b32 v57, v35, v39 offset0:192 offset1:193
	ds_write_b32 v57, v43 offset:776
	ds_read_b128 v[8:11], v2
	ds_read_b128 v[12:15], v2 offset:1024
	ds_read_b128 v[16:19], v2 offset:2048
	ds_read_b128 v[20:23], v2 offset:3072
	ds_read_b128 v[24:27], v2 offset:4096
	ds_read_b128 v[28:31], v2 offset:5120
	s_waitcnt lgkmcnt(0)
	global_store_dwordx4 v1, v[8:11], s[10:11] offset:-2048 sc1 nt
	global_store_dwordx4 v1, v[12:15], s[10:11] offset:-1024 sc1 nt
	global_store_dwordx4 v1, v[16:19], s[10:11] offset:0 sc1 nt
	global_store_dwordx4 v1, v[20:23], s[10:11] offset:1024 sc1 nt
	global_store_dwordx4 v1, v[24:27], s[10:11] offset:2048 sc1 nt
	s_and_saveexec_b64 s[16:17], s[14:15]
	global_store_dwordx4 v1, v[28:31], s[10:11] offset:3072 sc1 nt
	s_endpgm
